# U3f tail-tile prefetch: the 53 double-duty waves issue their second tile row loads before the first tile MFMA chains
# speedup vs baseline: 1.0024x; 1.0024x over previous
.Lu3_again:
	s_load_dword s3, s[0:1], 0x58
	v_lshrrev_b32_e32 v1, 6, v0
	s_waitcnt lgkmcnt(0)
	v_lshl_add_u32 v1, s2, 2, v1
	v_add_u32_e32 v1, s31, v1
	s_movk_i32 s2, 0xc35
	v_cmp_gt_i32_e32 vcc, s2, v1
	s_and_saveexec_b64 s[2:3], vcc
	s_cbranch_execz .LBB9_4
	s_load_dwordx4 s[4:7], s[0:1], 0x30
	s_load_dwordx2 s[2:3], s[0:1], 0x40
	s_load_dwordx4 s[8:11], s[0:1], 0x0
	v_and_b32_e32 v22, 31, v0
	v_lshlrev_b32_e32 v1, 5, v1
	v_or_b32_e32 v2, v1, v22
	v_ashrrev_i32_e32 v3, 31, v2
	v_lshlrev_b64 v[16:17], 7, v[2:3]
	v_and_b32_e32 v4, 32, v0
	s_waitcnt lgkmcnt(0)
	v_lshl_add_u64 v[2:3], s[10:11], 0, v[16:17]
	v_lshlrev_b32_e32 v28, 1, v4
	v_mov_b32_e32 v29, 0
	v_lshl_add_u64 v[18:19], v[2:3], 0, v[28:29]
	s_waitcnt vmcnt(0)
	v_mov_b32_e32 v2, v44
	v_mov_b32_e32 v3, v45
	v_mov_b32_e32 v4, v46
	v_mov_b32_e32 v5, v47
	v_mov_b32_e32 v6, v48
	v_mov_b32_e32 v7, v49
	v_mov_b32_e32 v8, v50
	v_mov_b32_e32 v9, v51
	v_mov_b32_e32 v12, v52
	v_mov_b32_e32 v13, v53
	v_mov_b32_e32 v14, v54
	v_mov_b32_e32 v15, v55
	v_mov_b32_e32 v24, v56
	v_mov_b32_e32 v25, v57
	v_mov_b32_e32 v26, v58
	v_mov_b32_e32 v27, v59
	v_lshl_add_u64 v[16:17], s[8:9], 0, v[16:17]
	v_lshl_add_u64 v[16:17], v[16:17], 0, v[28:29]
	v_and_b32_e32 v76, 0x80, v10
	v_and_b32_e32 v20, 63, v0
	v_lshrrev_b32_e32 v0, 3, v0
	v_and_or_b32 v0, v0, 4, v1
	v_ashrrev_i32_e32 v1, 31, v0
	s_waitcnt vmcnt(0)
	v_mov_b32_e32 v28, v60
	v_mov_b32_e32 v29, v61
	v_mov_b32_e32 v30, v62
	v_mov_b32_e32 v31, v63
	v_mov_b32_e32 v32, v64
	v_mov_b32_e32 v33, v65
	v_mov_b32_e32 v34, v66
	v_mov_b32_e32 v35, v67
	v_mov_b32_e32 v36, v68
	v_mov_b32_e32 v37, v69
	v_mov_b32_e32 v38, v70
	v_mov_b32_e32 v39, v71
	v_mov_b32_e32 v40, v72
	v_mov_b32_e32 v41, v73
	v_mov_b32_e32 v42, v74
	v_mov_b32_e32 v43, v75
	v_cvt_f32_f16_sdwa v17, v24 dst_sel:DWORD dst_unused:UNUSED_PAD src0_sel:WORD_1
	s_waitcnt vmcnt(0)
	v_lshlrev_b32_e32 v11, 16, v40
	v_and_b32_e32 v16, 0xffff0000, v40
	v_lshlrev_b32_e32 v21, 16, v41
	v_and_b32_e32 v23, 0xffff0000, v41
	v_lshlrev_b32_e32 v48, 16, v42
	v_and_b32_e32 v49, 0xffff0000, v42
	v_lshlrev_b32_e32 v50, 16, v43
	v_and_b32_e32 v51, 0xffff0000, v43
	v_lshlrev_b32_e32 v52, 16, v36
	v_and_b32_e32 v53, 0xffff0000, v36
	v_lshlrev_b32_e32 v54, 16, v37
	v_and_b32_e32 v55, 0xffff0000, v37
	v_lshlrev_b32_e32 v56, 16, v38
	v_and_b32_e32 v57, 0xffff0000, v38
	v_lshlrev_b32_e32 v58, 16, v39
	v_and_b32_e32 v59, 0xffff0000, v39
	v_lshlrev_b32_e32 v60, 16, v32
	v_and_b32_e32 v61, 0xffff0000, v32
	v_lshlrev_b32_e32 v62, 16, v33
	v_and_b32_e32 v63, 0xffff0000, v33
	v_lshlrev_b32_e32 v64, 16, v34
	v_and_b32_e32 v65, 0xffff0000, v34
	v_lshlrev_b32_e32 v66, 16, v35
	v_and_b32_e32 v67, 0xffff0000, v35
	v_lshlrev_b32_e32 v68, 16, v28
	v_and_b32_e32 v69, 0xffff0000, v28
	v_lshlrev_b32_e32 v70, 16, v29
	v_and_b32_e32 v71, 0xffff0000, v29
	v_lshlrev_b32_e32 v72, 16, v30
	v_and_b32_e32 v73, 0xffff0000, v30
	v_lshlrev_b32_e32 v74, 16, v31
	v_and_b32_e32 v75, 0xffff0000, v31
	ds_read_b128 v[28:31], v76 offset:32768
	ds_read_b128 v[32:35], v76 offset:32784
	ds_read_b128 v[36:39], v76 offset:32800
	ds_read_b128 v[40:43], v76 offset:32816
	ds_read_b128 v[44:47], v76 offset:33024
	s_waitcnt lgkmcnt(0)
	v_fma_f32 v10, v28, v11, v44
	v_fma_f32 v11, v29, v16, v45
	v_cvt_f32_f16_e32 v16, v24
	v_max_f32_e32 v10, 0, v10
	v_max_f32_e32 v11, 0, v11
	v_fmac_f32_e32 v47, v31, v23
	v_pk_add_f32 v[44:45], v[10:11], v[16:17]
	v_cvt_f32_f16_e32 v16, v25
	v_cvt_f32_f16_sdwa v17, v25 dst_sel:DWORD dst_unused:UNUSED_PAD src0_sel:WORD_1
	v_fma_f32 v10, v30, v21, v46
	ds_read_b128 v[28:31], v76 offset:33040
	v_max_f32_e32 v10, 0, v10
	v_max_f32_e32 v11, 0, v47
	v_pk_add_f32 v[46:47], v[10:11], v[16:17]
	v_cvt_f32_f16_e32 v16, v26
	v_cvt_f32_f16_sdwa v17, v26 dst_sel:DWORD dst_unused:UNUSED_PAD src0_sel:WORD_1
	s_waitcnt lgkmcnt(0)
	v_fma_f32 v10, v32, v48, v28
	v_fma_f32 v11, v33, v49, v29
	v_max_f32_e32 v10, 0, v10
	v_max_f32_e32 v11, 0, v11
	v_pk_add_f32 v[28:29], v[10:11], v[16:17]
	v_cvt_f32_f16_e32 v16, v27
	v_cvt_f32_f16_sdwa v17, v27 dst_sel:DWORD dst_unused:UNUSED_PAD src0_sel:WORD_1
	ds_read_b128 v[24:27], v76 offset:33056
	v_fma_f32 v10, v34, v50, v30
	v_fmac_f32_e32 v31, v35, v51
	v_max_f32_e32 v10, 0, v10
	v_max_f32_e32 v11, 0, v31
	v_pk_add_f32 v[30:31], v[10:11], v[16:17]
	v_cvt_f32_f16_e32 v16, v12
	v_cvt_f32_f16_sdwa v17, v12 dst_sel:DWORD dst_unused:UNUSED_PAD src0_sel:WORD_1
	s_waitcnt lgkmcnt(0)
	v_fma_f32 v10, v36, v52, v24
	v_fma_f32 v11, v37, v53, v25
	v_cvt_f32_f16_e32 v12, v13
	v_cvt_f32_f16_sdwa v13, v13 dst_sel:DWORD dst_unused:UNUSED_PAD src0_sel:WORD_1
	v_max_f32_e32 v10, 0, v10
	v_max_f32_e32 v11, 0, v11
	v_pk_add_f32 v[24:25], v[10:11], v[16:17]
	v_fma_f32 v10, v38, v54, v26
	v_fmac_f32_e32 v27, v39, v55
	v_max_f32_e32 v10, 0, v10
	v_max_f32_e32 v11, 0, v27
	v_pk_add_f32 v[26:27], v[10:11], v[12:13]
	ds_read_b128 v[10:13], v76 offset:33072
	v_cvt_f32_f16_e32 v16, v14
	v_cvt_f32_f16_sdwa v17, v14 dst_sel:DWORD dst_unused:UNUSED_PAD src0_sel:WORD_1
	v_lshlrev_b32_e32 v23, 4, v20
	s_waitcnt lgkmcnt(0)
	v_fma_f32 v10, v40, v56, v10
	v_fma_f32 v11, v41, v57, v11
	v_max_f32_e32 v10, 0, v10
	v_max_f32_e32 v11, 0, v11
	v_fmac_f32_e32 v13, v43, v59
	v_pk_add_f32 v[32:33], v[10:11], v[16:17]
	v_fma_f32 v10, v42, v58, v12
	v_max_f32_e32 v11, 0, v13
	v_cvt_f32_f16_e32 v12, v15
	v_cvt_f32_f16_sdwa v13, v15 dst_sel:DWORD dst_unused:UNUSED_PAD src0_sel:WORD_1
	v_max_f32_e32 v10, 0, v10
	v_pk_add_f32 v[34:35], v[10:11], v[12:13]
	ds_read_b128 v[10:13], v76 offset:32832
	ds_read_b128 v[14:17], v76 offset:33088
	s_waitcnt lgkmcnt(0)
	v_fma_f32 v10, v10, v60, v14
	v_fma_f32 v11, v11, v61, v15
	v_cvt_f32_f16_e32 v14, v6
	v_cvt_f32_f16_sdwa v15, v6 dst_sel:DWORD dst_unused:UNUSED_PAD src0_sel:WORD_1
	v_max_f32_e32 v10, 0, v10
	v_max_f32_e32 v11, 0, v11
	v_fma_f32 v6, v12, v62, v16
	v_pk_add_f32 v[36:37], v[10:11], v[14:15]
	v_max_f32_e32 v10, 0, v6
	v_cvt_f32_f16_e32 v6, v7
	v_cvt_f32_f16_sdwa v7, v7 dst_sel:DWORD dst_unused:UNUSED_PAD src0_sel:WORD_1
	v_fmac_f32_e32 v17, v13, v63
	v_max_f32_e32 v11, 0, v17
	v_pk_add_f32 v[38:39], v[10:11], v[6:7]
	ds_read_b128 v[10:13], v76 offset:32848
	ds_read_b128 v[14:17], v76 offset:33104
	s_waitcnt lgkmcnt(0)
	v_fma_f32 v6, v10, v64, v14
	v_fma_f32 v7, v11, v65, v15
	v_cvt_f32_f16_e32 v10, v8
	v_cvt_f32_f16_sdwa v11, v8 dst_sel:DWORD dst_unused:UNUSED_PAD src0_sel:WORD_1
	v_cvt_f32_f16_e32 v8, v9
	v_cvt_f32_f16_sdwa v9, v9 dst_sel:DWORD dst_unused:UNUSED_PAD src0_sel:WORD_1
	v_max_f32_e32 v6, 0, v6
	v_max_f32_e32 v7, 0, v7
	v_pk_add_f32 v[40:41], v[6:7], v[10:11]
	v_fma_f32 v6, v12, v66, v16
	v_fmac_f32_e32 v17, v13, v67
	v_max_f32_e32 v6, 0, v6
	v_max_f32_e32 v7, 0, v17
	v_pk_add_f32 v[42:43], v[6:7], v[8:9]
	ds_read_b128 v[6:9], v76 offset:32864
	ds_read_b128 v[10:13], v76 offset:33120
	v_cvt_pk_f16_f32 v14, v44, v45
	v_cvt_pk_f16_f32 v15, v46, v47
	v_cvt_pk_f16_f32 v16, v28, v29
	v_cvt_pk_f16_f32 v17, v30, v31
	s_waitcnt lgkmcnt(0)
	v_fma_f32 v6, v6, v68, v10
	v_fma_f32 v7, v7, v69, v11
	v_cvt_f32_f16_e32 v10, v2
	v_cvt_f32_f16_sdwa v11, v2 dst_sel:DWORD dst_unused:UNUSED_PAD src0_sel:WORD_1
	v_max_f32_e32 v6, 0, v6
	v_max_f32_e32 v7, 0, v7
	v_fma_f32 v2, v8, v70, v12
	v_pk_add_f32 v[48:49], v[6:7], v[10:11]
	v_max_f32_e32 v6, 0, v2
	v_cvt_f32_f16_e32 v2, v3
	v_cvt_f32_f16_sdwa v3, v3 dst_sel:DWORD dst_unused:UNUSED_PAD src0_sel:WORD_1
	v_fmac_f32_e32 v13, v9, v71
	v_max_f32_e32 v7, 0, v13
	v_pk_add_f32 v[50:51], v[6:7], v[2:3]
	ds_read_b128 v[6:9], v76 offset:32880
	ds_read_b128 v[10:13], v76 offset:33136
	global_store_dwordx4 v[18:19], v[14:17], off
	s_waitcnt lgkmcnt(0)
	v_fma_f32 v2, v6, v72, v10
	v_fma_f32 v3, v7, v73, v11
	v_cvt_f32_f16_e32 v6, v4
	v_cvt_f32_f16_sdwa v7, v4 dst_sel:DWORD dst_unused:UNUSED_PAD src0_sel:WORD_1
	v_cvt_f32_f16_e32 v4, v5
	v_cvt_f32_f16_sdwa v5, v5 dst_sel:DWORD dst_unused:UNUSED_PAD src0_sel:WORD_1
	v_max_f32_e32 v2, 0, v2
	v_max_f32_e32 v3, 0, v3
	v_pk_add_f32 v[52:53], v[2:3], v[6:7]
	v_fma_f32 v2, v8, v74, v12
	v_fmac_f32_e32 v13, v9, v75
	v_max_f32_e32 v2, 0, v2
	v_max_f32_e32 v3, 0, v13
	v_pk_add_f32 v[54:55], v[2:3], v[4:5]
	v_cvt_pk_f16_f32 v10, v24, v25
	v_cvt_pk_f16_f32 v11, v26, v27
	v_cvt_pk_f16_f32 v12, v32, v33
	v_cvt_pk_f16_f32 v13, v34, v35
	v_cvt_pk_f16_f32 v6, v36, v37
	v_cvt_pk_f16_f32 v7, v38, v39
	v_cvt_pk_f16_f32 v8, v40, v41
	v_cvt_pk_f16_f32 v9, v42, v43
	v_cvt_pk_f16_f32 v2, v48, v49
	v_cvt_pk_f16_f32 v3, v50, v51
	v_cvt_pk_f16_f32 v4, v52, v53
	v_cvt_pk_f16_f32 v5, v54, v55
	global_store_dwordx4 v[18:19], v[10:13], off offset:16
	global_store_dwordx4 v[18:19], v[6:9], off offset:32
	global_store_dwordx4 v[18:19], v[2:5], off offset:48
	v_lshlrev_b32_e32 v18, 3, v22
	global_load_dwordx2 a[0:1], v18, s[4:5]
	ds_read_b128 v[18:21], v23
	ds_read_b128 v[24:27], v23 offset:8192
	ds_read_b128 v[28:31], v23 offset:4096
	ds_read_b128 v[32:35], v23 offset:12288
	s_waitcnt vmcnt(0)
	s_cmp_lg_u32 s31, 0
	s_cbranch_scc1 .Lu3_nopf
	v_lshrrev_b32_e32 v78, 6, v77
	s_lshl_b32 s33, s30, 2
	v_readfirstlane_b32 s32, v78
	s_add_i32 s32, s32, s33
	s_cmp_ge_u32 s32, 53
	s_cbranch_scc1 .Lu3_nopf
	s_add_i32 s32, s32, 0xc00
	s_lshl_b32 s32, s32, 5
	v_and_b32_e32 v78, 31, v77
	v_or_b32_e32 v78, s32, v78
	v_lshlrev_b32_e32 v78, 7, v78
	v_and_b32_e32 v76, 32, v77
	v_lshl_add_u32 v78, v76, 1, v78
	global_load_dwordx4 v[44:47], v78, s[22:23] offset:48
	global_load_dwordx4 v[48:51], v78, s[22:23] offset:32
	global_load_dwordx4 v[52:55], v78, s[22:23] offset:16
	global_load_dwordx4 v[56:59], v78, s[22:23]
	global_load_dwordx4 v[60:63], v78, s[20:21] offset:48
	global_load_dwordx4 v[64:67], v78, s[20:21] offset:32
	global_load_dwordx4 v[68:71], v78, s[20:21] offset:16
	global_load_dwordx4 v[72:75], v78, s[20:21]
.Lu3_nopf:
	v_accvgpr_mov_b32 a16, a0
	v_accvgpr_mov_b32 a17, a0
	v_accvgpr_mov_b32 a18, a0
	v_accvgpr_mov_b32 a19, a0
	v_accvgpr_mov_b32 a20, a0
	v_accvgpr_mov_b32 a21, a0
	v_accvgpr_mov_b32 a22, a0
	v_accvgpr_mov_b32 a23, a0
	v_accvgpr_mov_b32 a24, a0
	v_accvgpr_mov_b32 a25, a0
	v_accvgpr_mov_b32 a26, a0
	v_accvgpr_mov_b32 a27, a0
	v_accvgpr_mov_b32 a28, a0
	v_accvgpr_mov_b32 a29, a0
	v_accvgpr_mov_b32 a30, a0
	v_accvgpr_mov_b32 a31, a0
	v_accvgpr_mov_b32 a0, a1
	v_accvgpr_mov_b32 a2, a1
	v_accvgpr_mov_b32 a3, a1
	v_accvgpr_mov_b32 a4, a1
	v_accvgpr_mov_b32 a5, a1
	v_accvgpr_mov_b32 a6, a1
	v_accvgpr_mov_b32 a7, a1
	v_accvgpr_mov_b32 a8, a1
	v_accvgpr_mov_b32 a9, a1
	v_accvgpr_mov_b32 a10, a1
	v_accvgpr_mov_b32 a11, a1
	v_accvgpr_mov_b32 a12, a1
	v_accvgpr_mov_b32 a13, a1
	v_accvgpr_mov_b32 a14, a1
	v_accvgpr_mov_b32 a15, a1
	s_waitcnt lgkmcnt(3)
	v_mfma_f32_32x32x16_f16 a[16:31], v[14:17], v[18:21], a[16:31]
	s_waitcnt lgkmcnt(1)
	v_mfma_f32_32x32x16_f16 a[0:15], v[14:17], v[28:31], a[0:15]
	v_mfma_f32_32x32x16_f16 a[16:31], v[14:17], v[24:27], a[16:31]
	s_waitcnt lgkmcnt(0)
	v_mfma_f32_32x32x16_f16 a[0:15], v[14:17], v[32:35], a[0:15]
	ds_read_b128 v[18:21], v23 offset:1024
	ds_read_b128 v[24:27], v23 offset:9216
	ds_read_b128 v[28:31], v23 offset:5120
	ds_read_b128 v[32:35], v23 offset:13312
	s_waitcnt lgkmcnt(3)
	v_mfma_f32_32x32x16_f16 a[16:31], v[10:13], v[18:21], a[16:31]
	s_waitcnt lgkmcnt(1)
	v_mfma_f32_32x32x16_f16 a[0:15], v[10:13], v[28:31], a[0:15]
	v_mfma_f32_32x32x16_f16 a[16:31], v[10:13], v[24:27], a[16:31]
	s_waitcnt lgkmcnt(0)
	v_mfma_f32_32x32x16_f16 a[0:15], v[10:13], v[32:35], a[0:15]
	ds_read_b128 v[18:21], v23 offset:2048
	ds_read_b128 v[24:27], v23 offset:10240
	ds_read_b128 v[28:31], v23 offset:6144
	ds_read_b128 v[32:35], v23 offset:14336
	s_waitcnt lgkmcnt(3)
	v_mfma_f32_32x32x16_f16 a[16:31], v[6:9], v[18:21], a[16:31]
	s_waitcnt lgkmcnt(1)
	v_mfma_f32_32x32x16_f16 a[0:15], v[6:9], v[28:31], a[0:15]
	v_mfma_f32_32x32x16_f16 a[16:31], v[6:9], v[24:27], a[16:31]
	s_waitcnt lgkmcnt(0)
	v_mfma_f32_32x32x16_f16 a[0:15], v[6:9], v[32:35], a[0:15]
	ds_read_b128 v[18:21], v23 offset:3072
	ds_read_b128 v[24:27], v23 offset:11264
	ds_read_b128 v[28:31], v23 offset:7168
	ds_read_b128 v[32:35], v23 offset:15360
	s_waitcnt lgkmcnt(3)
	v_mfma_f32_32x32x16_f16 a[16:31], v[2:5], v[18:21], a[16:31]
	s_waitcnt lgkmcnt(1)
	v_mfma_f32_32x32x16_f16 a[0:15], v[2:5], v[28:31], a[0:15]
	v_mfma_f32_32x32x16_f16 a[16:31], v[2:5], v[24:27], a[16:31]
	s_waitcnt lgkmcnt(0)
	v_mfma_f32_32x32x16_f16 a[0:15], v[2:5], v[32:35], a[0:15]
	ds_read_b128 v[18:21], v23 offset:16384
	ds_read_b128 v[24:27], v23 offset:24576
	ds_read_b128 v[28:31], v23 offset:20480
	ds_read_b128 v[32:35], v23 offset:28672
	s_waitcnt lgkmcnt(3)
	v_mfma_f32_32x32x16_f16 a[32:47], v[14:17], v[18:21], 0
	s_waitcnt lgkmcnt(1)
	v_mfma_f32_32x32x16_f16 a[48:63], v[14:17], v[28:31], 0
	v_mfma_f32_32x32x16_f16 a[32:47], v[14:17], v[24:27], a[32:47]
	s_waitcnt lgkmcnt(0)
	v_mfma_f32_32x32x16_f16 a[48:63], v[14:17], v[32:35], a[48:63]
	ds_read_b128 v[14:17], v23 offset:17408
	ds_read_b128 v[18:21], v23 offset:25600
	ds_read_b128 v[24:27], v23 offset:21504
	ds_read_b128 v[28:31], v23 offset:29696
	s_waitcnt lgkmcnt(3)
	v_mfma_f32_32x32x16_f16 a[32:47], v[10:13], v[14:17], a[32:47]
	s_waitcnt lgkmcnt(1)
	v_mfma_f32_32x32x16_f16 a[48:63], v[10:13], v[24:27], a[48:63]
	v_mfma_f32_32x32x16_f16 a[32:47], v[10:13], v[18:21], a[32:47]
	s_waitcnt lgkmcnt(0)
	v_mfma_f32_32x32x16_f16 a[48:63], v[10:13], v[28:31], a[48:63]
	ds_read_b128 v[10:13], v23 offset:18432
	ds_read_b128 v[14:17], v23 offset:26624
	ds_read_b128 v[18:21], v23 offset:22528
	ds_read_b128 v[24:27], v23 offset:30720
	s_waitcnt lgkmcnt(3)
	v_mfma_f32_32x32x16_f16 a[32:47], v[6:9], v[10:13], a[32:47]
	s_waitcnt lgkmcnt(1)
	v_mfma_f32_32x32x16_f16 a[48:63], v[6:9], v[18:21], a[48:63]
	v_mfma_f32_32x32x16_f16 a[32:47], v[6:9], v[14:17], a[32:47]
	s_waitcnt lgkmcnt(0)
	v_mfma_f32_32x32x16_f16 a[48:63], v[6:9], v[24:27], a[48:63]
	ds_read_b128 v[10:13], v23 offset:19456
	ds_read_b128 v[6:9], v23 offset:27648
	ds_read_b128 v[18:21], v23 offset:23552
	ds_read_b128 v[14:17], v23 offset:31744
	s_waitcnt lgkmcnt(3)
	v_mfma_f32_32x32x16_f16 a[32:47], v[2:5], v[10:13], a[32:47]
	s_waitcnt lgkmcnt(1)
	v_mfma_f32_32x32x16_f16 a[48:63], v[2:5], v[18:21], a[48:63]
	v_mfma_f32_32x32x16_f16 a[32:47], v[2:5], v[6:9], a[32:47]
	v_lshlrev_b32_e32 v7, 2, v22
	s_waitcnt lgkmcnt(0)
	v_mfma_f32_32x32x16_f16 a[48:63], v[2:5], v[14:17], a[48:63]
	v_accvgpr_read_b32 v2, a0
	v_accvgpr_read_b32 v3, a16
	v_cvt_pk_bf16_f32 v6, v3, v2
	v_lshlrev_b64 v[2:3], 7, v[0:1]
	v_or_b32_e32 v2, v2, v7
	v_lshl_add_u64 v[4:5], s[6:7], 0, v[2:3]
	global_store_dword v[4:5], v6, off
	s_nop 1
	v_accvgpr_read_b32 v4, a32
	v_lshl_add_u64 v[2:3], s[2:3], 0, v[2:3]
	s_nop 0
	v_accvgpr_read_b32 v1, a48
	v_cvt_pk_bf16_f32 v1, v4, v1
	global_store_dword v[2:3], v1, off
	v_or_b32_e32 v2, 1, v0
	v_ashrrev_i32_e32 v3, 31, v2
	v_lshlrev_b64 v[2:3], 7, v[2:3]
	v_accvgpr_read_b32 v1, a1
	v_accvgpr_read_b32 v4, a17
	v_or_b32_e32 v2, v2, v7
	v_cvt_pk_bf16_f32 v1, v4, v1
	v_lshl_add_u64 v[4:5], s[6:7], 0, v[2:3]
	global_store_dword v[4:5], v1, off
	v_accvgpr_read_b32 v1, a49
	v_accvgpr_read_b32 v4, a33
	v_cvt_pk_bf16_f32 v1, v4, v1
	v_lshl_add_u64 v[2:3], s[2:3], 0, v[2:3]
	global_store_dword v[2:3], v1, off
	v_or_b32_e32 v2, 2, v0
	v_ashrrev_i32_e32 v3, 31, v2
	v_lshlrev_b64 v[2:3], 7, v[2:3]
	v_accvgpr_read_b32 v1, a2
	v_accvgpr_read_b32 v4, a18
	v_or_b32_e32 v2, v2, v7
	v_cvt_pk_bf16_f32 v1, v4, v1
	v_lshl_add_u64 v[4:5], s[6:7], 0, v[2:3]
	global_store_dword v[4:5], v1, off
	v_accvgpr_read_b32 v1, a50
	v_accvgpr_read_b32 v4, a34
	v_cvt_pk_bf16_f32 v1, v4, v1
	v_lshl_add_u64 v[2:3], s[2:3], 0, v[2:3]
	global_store_dword v[2:3], v1, off
	v_or_b32_e32 v2, 3, v0
	v_ashrrev_i32_e32 v3, 31, v2
	v_lshlrev_b64 v[2:3], 7, v[2:3]
	v_accvgpr_read_b32 v1, a3
	v_accvgpr_read_b32 v4, a19
	v_or_b32_e32 v2, v2, v7
	v_cvt_pk_bf16_f32 v1, v4, v1
	v_lshl_add_u64 v[4:5], s[6:7], 0, v[2:3]
	global_store_dword v[4:5], v1, off
	v_accvgpr_read_b32 v1, a51
	v_accvgpr_read_b32 v4, a35
	v_cvt_pk_bf16_f32 v1, v4, v1
	v_lshl_add_u64 v[2:3], s[2:3], 0, v[2:3]
	global_store_dword v[2:3], v1, off
	v_or_b32_e32 v2, 8, v0
	v_ashrrev_i32_e32 v3, 31, v2
	v_lshlrev_b64 v[2:3], 7, v[2:3]
	v_accvgpr_read_b32 v1, a4
	v_accvgpr_read_b32 v4, a20
	v_or_b32_e32 v2, v2, v7
	v_cvt_pk_bf16_f32 v1, v4, v1
	v_lshl_add_u64 v[4:5], s[6:7], 0, v[2:3]
	global_store_dword v[4:5], v1, off
	v_accvgpr_read_b32 v1, a52
	v_accvgpr_read_b32 v4, a36
	v_cvt_pk_bf16_f32 v1, v4, v1
	v_lshl_add_u64 v[2:3], s[2:3], 0, v[2:3]
	global_store_dword v[2:3], v1, off
	v_or_b32_e32 v2, 9, v0
	v_ashrrev_i32_e32 v3, 31, v2
	v_lshlrev_b64 v[2:3], 7, v[2:3]
	v_accvgpr_read_b32 v1, a5
	v_accvgpr_read_b32 v4, a21
	v_or_b32_e32 v2, v2, v7
	v_cvt_pk_bf16_f32 v1, v4, v1
	v_lshl_add_u64 v[4:5], s[6:7], 0, v[2:3]
	global_store_dword v[4:5], v1, off
	v_accvgpr_read_b32 v1, a53
	v_accvgpr_read_b32 v4, a37
	v_cvt_pk_bf16_f32 v1, v4, v1
	v_lshl_add_u64 v[2:3], s[2:3], 0, v[2:3]
	global_store_dword v[2:3], v1, off
	v_or_b32_e32 v2, 10, v0
	v_ashrrev_i32_e32 v3, 31, v2
	v_lshlrev_b64 v[2:3], 7, v[2:3]
	v_accvgpr_read_b32 v1, a6
	v_accvgpr_read_b32 v4, a22
	v_or_b32_e32 v2, v2, v7
	v_cvt_pk_bf16_f32 v1, v4, v1
	v_lshl_add_u64 v[4:5], s[6:7], 0, v[2:3]
	global_store_dword v[4:5], v1, off
	v_accvgpr_read_b32 v1, a54
	v_accvgpr_read_b32 v4, a38
	v_cvt_pk_bf16_f32 v1, v4, v1
	v_lshl_add_u64 v[2:3], s[2:3], 0, v[2:3]
	global_store_dword v[2:3], v1, off
	v_or_b32_e32 v2, 11, v0
	v_ashrrev_i32_e32 v3, 31, v2
	v_lshlrev_b64 v[2:3], 7, v[2:3]
	v_accvgpr_read_b32 v1, a7
	v_accvgpr_read_b32 v4, a23
	v_or_b32_e32 v2, v2, v7
	v_cvt_pk_bf16_f32 v1, v4, v1
	v_lshl_add_u64 v[4:5], s[6:7], 0, v[2:3]
	global_store_dword v[4:5], v1, off
	v_accvgpr_read_b32 v1, a55
	v_accvgpr_read_b32 v4, a39
	v_cvt_pk_bf16_f32 v1, v4, v1
	v_lshl_add_u64 v[2:3], s[2:3], 0, v[2:3]
	global_store_dword v[2:3], v1, off
	v_or_b32_e32 v2, 16, v0
	v_ashrrev_i32_e32 v3, 31, v2
	v_lshlrev_b64 v[2:3], 7, v[2:3]
	v_accvgpr_read_b32 v1, a8
	v_accvgpr_read_b32 v4, a24
	v_or_b32_e32 v2, v2, v7
	v_cvt_pk_bf16_f32 v1, v4, v1
	v_lshl_add_u64 v[4:5], s[6:7], 0, v[2:3]
	global_store_dword v[4:5], v1, off
	v_accvgpr_read_b32 v1, a56
	v_accvgpr_read_b32 v4, a40
	v_cvt_pk_bf16_f32 v1, v4, v1
	v_lshl_add_u64 v[2:3], s[2:3], 0, v[2:3]
	global_store_dword v[2:3], v1, off
	v_or_b32_e32 v2, 17, v0
	v_ashrrev_i32_e32 v3, 31, v2
	v_lshlrev_b64 v[2:3], 7, v[2:3]
	v_accvgpr_read_b32 v1, a9
	v_accvgpr_read_b32 v4, a25
	v_or_b32_e32 v2, v2, v7
	v_cvt_pk_bf16_f32 v1, v4, v1
	v_lshl_add_u64 v[4:5], s[6:7], 0, v[2:3]
	global_store_dword v[4:5], v1, off
	v_accvgpr_read_b32 v1, a57
	v_accvgpr_read_b32 v4, a41
	v_cvt_pk_bf16_f32 v1, v4, v1
	v_lshl_add_u64 v[2:3], s[2:3], 0, v[2:3]
	global_store_dword v[2:3], v1, off
	v_or_b32_e32 v2, 18, v0
	v_ashrrev_i32_e32 v3, 31, v2
	v_lshlrev_b64 v[2:3], 7, v[2:3]
	v_accvgpr_read_b32 v1, a10
	v_accvgpr_read_b32 v4, a26
	v_or_b32_e32 v2, v2, v7
	v_cvt_pk_bf16_f32 v1, v4, v1
	v_lshl_add_u64 v[4:5], s[6:7], 0, v[2:3]
	global_store_dword v[4:5], v1, off
	v_accvgpr_read_b32 v1, a58
	v_accvgpr_read_b32 v4, a42
	v_cvt_pk_bf16_f32 v1, v4, v1
	v_lshl_add_u64 v[2:3], s[2:3], 0, v[2:3]
	global_store_dword v[2:3], v1, off
	v_or_b32_e32 v2, 19, v0
	v_ashrrev_i32_e32 v3, 31, v2
	v_lshlrev_b64 v[2:3], 7, v[2:3]
	v_accvgpr_read_b32 v1, a11
	v_accvgpr_read_b32 v4, a27
	v_or_b32_e32 v2, v2, v7
	v_cvt_pk_bf16_f32 v1, v4, v1
	v_lshl_add_u64 v[4:5], s[6:7], 0, v[2:3]
	global_store_dword v[4:5], v1, off
	v_accvgpr_read_b32 v1, a59
	v_accvgpr_read_b32 v4, a43
	v_cvt_pk_bf16_f32 v1, v4, v1
	v_lshl_add_u64 v[2:3], s[2:3], 0, v[2:3]
	global_store_dword v[2:3], v1, off
	v_or_b32_e32 v2, 24, v0
	v_ashrrev_i32_e32 v3, 31, v2
	v_lshlrev_b64 v[2:3], 7, v[2:3]
	v_accvgpr_read_b32 v1, a12
	v_accvgpr_read_b32 v4, a28
	v_or_b32_e32 v2, v2, v7
	v_cvt_pk_bf16_f32 v1, v4, v1
	v_lshl_add_u64 v[4:5], s[6:7], 0, v[2:3]
	global_store_dword v[4:5], v1, off
	v_accvgpr_read_b32 v1, a60
	v_accvgpr_read_b32 v4, a44
	v_cvt_pk_bf16_f32 v1, v4, v1
	v_lshl_add_u64 v[2:3], s[2:3], 0, v[2:3]
	global_store_dword v[2:3], v1, off
	v_or_b32_e32 v2, 25, v0
	v_ashrrev_i32_e32 v3, 31, v2
	v_lshlrev_b64 v[2:3], 7, v[2:3]
	v_accvgpr_read_b32 v1, a13
	v_accvgpr_read_b32 v4, a29
	v_or_b32_e32 v2, v2, v7
	v_cvt_pk_bf16_f32 v1, v4, v1
	v_lshl_add_u64 v[4:5], s[6:7], 0, v[2:3]
	global_store_dword v[4:5], v1, off
	v_accvgpr_read_b32 v1, a61
	v_accvgpr_read_b32 v4, a45
	v_cvt_pk_bf16_f32 v1, v4, v1
	v_lshl_add_u64 v[2:3], s[2:3], 0, v[2:3]
	global_store_dword v[2:3], v1, off
	v_or_b32_e32 v2, 26, v0
	v_ashrrev_i32_e32 v3, 31, v2
	v_lshlrev_b64 v[2:3], 7, v[2:3]
	v_accvgpr_read_b32 v1, a14
	v_accvgpr_read_b32 v4, a30
	v_or_b32_e32 v2, v2, v7
	v_cvt_pk_bf16_f32 v1, v4, v1
	v_lshl_add_u64 v[4:5], s[6:7], 0, v[2:3]
	global_store_dword v[4:5], v1, off
	v_accvgpr_read_b32 v1, a62
	v_accvgpr_read_b32 v4, a46
	v_cvt_pk_bf16_f32 v1, v4, v1
	v_lshl_add_u64 v[2:3], s[2:3], 0, v[2:3]
	v_or_b32_e32 v0, 27, v0
	global_store_dword v[2:3], v1, off
	v_ashrrev_i32_e32 v1, 31, v0
	v_lshlrev_b64 v[0:1], 7, v[0:1]
	v_accvgpr_read_b32 v2, a15
	v_accvgpr_read_b32 v3, a31
	v_or_b32_e32 v0, v0, v7
	v_cvt_pk_bf16_f32 v4, v3, v2
	v_lshl_add_u64 v[2:3], s[6:7], 0, v[0:1]
	global_store_dword v[2:3], v4, off
	v_accvgpr_read_b32 v2, a63
	v_accvgpr_read_b32 v3, a47
	v_cvt_pk_bf16_f32 v2, v3, v2
	v_lshl_add_u64 v[0:1], s[2:3], 0, v[0:1]
	global_store_dword v[0:1], v2, off
	s_cmp_lg_u32 s31, 0
	s_cbranch_scc1 .LBB9_4
	s_mov_b64 exec, -1
	v_lshrrev_b32_e32 v78, 6, v77
	s_lshl_b32 s33, s30, 2
	v_readfirstlane_b32 s32, v78
	s_add_i32 s32, s32, s33
	s_cmp_ge_u32 s32, 53
	s_cbranch_scc1 .LBB9_4
	s_movk_i32 s31, 0xc00
	s_mov_b32 s2, s30
	v_mov_b32_e32 v0, v77
	v_mov_b32_e32 v10, v79
	s_waitcnt vmcnt(0)
	s_branch .Lu3_again
